# MLA steady loops: waves 0-3 issue waves 4-7's two DMA pieces in their barrier slack (behind the PV section); waves 4-7 issue none
# speedup vs baseline: 1.0016x; 1.0016x over previous
; template <bool FOX>
; __device__ __forceinline__ void attn_unit(const Args& A, int b, int h, int qb, LAS char* shm, LAS float* dg) {
;     ...
;     for (int t = 1; t < t_end; ++t) {
;         if (t == 1 && 4 < nti) ISSUE_K(t0 + 4, 0);
;         if (t + 4 < nti) ISSUE_K(t0 + t + 4, t % NS);
;         if (t + 2 < nti) ISSUE_V(t0 + t + 2, (t + 2) % NS);
;         SFENCE();
;         { if constexpr (!FOX) { if (t0 + t == tw_last + 1) {
; #pragma unroll
;                   for (int r = 0; r < 16; ++r) negm[r] = -INFINITY;
;                   asm volatile("" : "+v"(negm)); } }
;           const lds_cptr vp = vp0 + ((t - 1) % NS) * VSLOT; float sa = 0.f, sb = 0.f;
; #pragma unroll
;           for (int g = 0; g < 2 * NQ; ++g) {
;               if (!FOX && g == 0) c0 = __builtin_amdgcn_mfma_f32_32x32x16_bf16(kf[0], qr[0], negm, 0, 0, 0);
;               else if (!FOX && g == 1) c1 = __builtin_amdgcn_mfma_f32_32x32x16_bf16(kf[1], qr[0], negm, 0, 0, 0);
;               else if (g & 1) c1 = __builtin_amdgcn_mfma_f32_32x32x16_bf16(kf[g], qr[g >> 1], c1, 0, 0, 0); else c0 = __builtin_amdgcn_mfma_f32_32x32x16_bf16(kf[g], qr[g >> 1], c0, 0, 0, 0);
;               if (g < 8) { const int i = (g >> 1) + 4 * (g & 1); vlo[i] = vtr(vp + (i >> 2) * 4096 + (i & 3) * 1024); vhi[i] = vtr(vp + (i >> 2) * 4096 + (i & 3) * 1024 + 512);
;                   if (g < 4) { sa += pp0[4 * g]; sb += pp0[4 * g + 1]; sa += pp0[4 * g + 2]; sb += pp0[4 * g + 3]; } else { sa += pp1[4 * g - 16]; sb += pp1[4 * g - 15]; sa += pp1[4 * g - 14]; sb += pp1[4 * g - 13]; }
;                   asm volatile("" : "+v"(sa), "+v"(sb)); }
;               { constexpr int G0 = FOX ? 0 : 4; if (g >= G0) { const int q = 2 * (g - G0);
; #pragma unroll
;                   for (int k = 0; k < 2; ++k) { const int w = q + k; const unsigned pkd = w < 8 ? cvt_pk_bf16(pp0[2 * w], pp0[2 * w + 1]) : cvt_pk_bf16(pp1[2 * w - 16], pp1[2 * w - 15]); pw[w >> 2][w & 3] = pkd; } } }
;               SFENCE();
;           }
;           lrun += sa + sb; }
;         MASKONLY(t);
;         float rm; ROWMAX(rm);
;         bool resc = false;
;         if (__any(rm > THR)) { const float dl = fmaxf(rm, 0.f); mhat += dl;
; #pragma unroll
;             for (int r = 0; r < 16; ++r) { c0[r] -= dl; c1[r] -= dl; }
;             if constexpr (!FOX) {
; #pragma unroll
;                 for (int r = 0; r < 16; ++r) negm[r] = -mhat;
.Lmla_ss1_in:
	s_mov_b32 m0, s52
	s_nop 0
	global_load_lds_dwordx4 v240, s[46:47]
	s_add_i32 m0, s52, 0x2000
	s_nop 0
	global_load_lds_dwordx4 v240, s[98:99]
	s_mov_b32 m0, s53
	s_nop 0
	global_load_lds_dwordx4 v240, s[60:61]
	s_waitcnt lgkmcnt(0)
	s_add_i32 s27, s42, 0x8000
	v_mfma_f32_32x32x16_bf16 v[114:129], v[206:209], v[138:141], v[82:97]
	s_and_b32 s27, s27, 0x6000
	s_add_u32 s42, s42, 0x2000
	s_addc_u32 s43, s43, 0
	v_add_u32_e32 v3, s27, v247
	ds_read_b64_tr_b16 v[206:207], v3 offset:49152
	ds_read_b64_tr_b16 v[208:209], v3 offset:49664
	v_add_f32_e32 v4, 0, v67
	v_add_f32_e32 v5, 0, v66
	v_add_f32_e32 v4, v69, v4
	v_add_f32_e32 v5, v68, v5
	v_mfma_f32_32x32x16_bf16 v[98:113], v[194:197], v[138:141], v[82:97]
	ds_read_b64_tr_b16 v[194:195], v3 offset:53248
	ds_read_b64_tr_b16 v[196:197], v3 offset:53760
	v_add_f32_e32 v4, v71, v4
	v_add_f32_e32 v5, v70, v5
	v_add_f32_e32 v4, v73, v4
	v_add_f32_e32 v5, v72, v5
	v_mfma_f32_32x32x16_bf16 v[114:129], v[202:205], v[142:145], v[114:129]
	ds_read_b64_tr_b16 v[202:203], v3 offset:50176
	ds_read_b64_tr_b16 v[204:205], v3 offset:50688
	v_add_f32_e32 v4, v75, v4
	v_add_f32_e32 v5, v74, v5
	v_add_f32_e32 v4, v77, v4
	v_add_f32_e32 v5, v76, v5
	v_mfma_f32_32x32x16_bf16 v[98:113], v[186:189], v[142:145], v[98:113]
	ds_read_b64_tr_b16 v[214:215], v3 offset:54272
	ds_read_b64_tr_b16 v[216:217], v3 offset:54784
	v_add_f32_e32 v4, v79, v4
	v_add_f32_e32 v5, v78, v5
	v_add_f32_e32 v4, v81, v4
	v_add_f32_e32 v5, v80, v5
	v_mfma_f32_32x32x16_bf16 v[114:129], v[198:201], v[146:149], v[114:129]
	ds_read_b64_tr_b16 v[210:211], v3 offset:51200
	ds_read_b64_tr_b16 v[212:213], v3 offset:51712
	v_add_f32_e32 v4, v51, v4
	v_add_f32_e32 v5, v50, v5
	v_add_f32_e32 v4, v53, v4
	v_add_f32_e32 v5, v52, v5
	v_mfma_f32_32x32x16_bf16 v[98:113], v[182:185], v[146:149], v[98:113]
	ds_read_b64_tr_b16 v[12:13], v3 offset:55296
	ds_read_b64_tr_b16 v[14:15], v3 offset:55808
	v_add_f32_e32 v4, v55, v4
	v_add_f32_e32 v5, v54, v5
	v_add_f32_e32 v4, v57, v4
	v_add_f32_e32 v5, v56, v5
	v_mfma_f32_32x32x16_bf16 v[114:129], v[190:193], v[150:153], v[114:129]
	ds_read_b64_tr_b16 v[8:9], v3 offset:52224
	ds_read_b64_tr_b16 v[10:11], v3 offset:52736
	v_add_f32_e32 v4, v59, v4
	v_add_f32_e32 v16, v61, v4
	v_add_f32_e32 v4, v58, v5
	v_add_f32_e32 v17, v60, v4
	v_mfma_f32_32x32x16_bf16 v[98:113], v[170:173], v[150:153], v[98:113]
	ds_read_b64_tr_b16 v[4:5], v3 offset:56320
	ds_read_b64_tr_b16 v[6:7], v3 offset:56832
	v_add_f32_e32 v3, v63, v16
	v_add_f32_e32 v16, v62, v17
	v_add_f32_e32 v3, v65, v3
	v_add_f32_e32 v16, v64, v16
	v_mfma_f32_32x32x16_bf16 v[114:129], v[178:181], v[154:157], v[114:129]
	v_cvt_pk_bf16_f32 v178, v50, v51
	v_cvt_pk_bf16_f32 v179, v52, v53
	v_cvt_pk_bf16_f32 v186, v66, v67
	v_cvt_pk_bf16_f32 v187, v68, v69
	v_mfma_f32_32x32x16_bf16 v[98:113], v[166:169], v[154:157], v[98:113]
	v_cvt_pk_bf16_f32 v180, v54, v55
	v_cvt_pk_bf16_f32 v181, v56, v57
	v_cvt_pk_bf16_f32 v188, v70, v71
	v_cvt_pk_bf16_f32 v189, v72, v73
	v_mfma_f32_32x32x16_bf16 v[114:129], v[174:177], v[158:161], v[114:129]
	v_cvt_pk_bf16_f32 v218, v58, v59
	v_cvt_pk_bf16_f32 v219, v60, v61
	v_cvt_pk_bf16_f32 v182, v74, v75
	v_cvt_pk_bf16_f32 v183, v76, v77
	v_mfma_f32_32x32x16_bf16 v[98:113], v[162:165], v[158:161], v[98:113]
	v_cvt_pk_bf16_f32 v220, v62, v63
	v_cvt_pk_bf16_f32 v221, v64, v65
	v_cvt_pk_bf16_f32 v184, v78, v79
	v_cvt_pk_bf16_f32 v185, v80, v81
	v_add_f32_e32 v3, v3, v16
	v_add_f32_e32 v246, v246, v3
	s_nop 3
	s_waitcnt lgkmcnt(0)
	v_mfma_f32_32x32x16_bf16 v[18:33], v[186:189], v[206:209], v[18:33]
	s_add_i32 s27, s26, 1
	s_and_b32 s64, s27, 3
	s_mulk_i32 s64, 0x3000
	v_exp_f32_e32 v66, v114
	v_exp_f32_e32 v67, v115
	v_exp_f32_e32 v68, v116
	v_exp_f32_e32 v69, v117
	v_add_u32_e32 v3, s64, v248
	v_mfma_f32_32x32x16_bf16 v[34:49], v[186:189], v[194:197], v[34:49]
	v_exp_f32_e32 v70, v118
	v_exp_f32_e32 v71, v119
	v_exp_f32_e32 v72, v120
	v_exp_f32_e32 v73, v121
	ds_read_b128 v[206:209], v3
	ds_read_b128 v[194:197], v3 offset:512
	v_mfma_f32_32x32x16_bf16 v[18:33], v[182:185], v[202:205], v[18:33]
	v_exp_f32_e32 v74, v122
	v_exp_f32_e32 v75, v123
	v_exp_f32_e32 v76, v124
	v_exp_f32_e32 v77, v125
	ds_read_b128 v[202:205], v3 offset:2048
	ds_read_b128 v[186:189], v3 offset:2560
	v_mfma_f32_32x32x16_bf16 v[34:49], v[182:185], v[214:217], v[34:49]
	v_exp_f32_e32 v78, v126
	v_exp_f32_e32 v79, v127
	v_exp_f32_e32 v80, v128
	v_exp_f32_e32 v81, v129
	ds_read_b128 v[198:201], v3 offset:4096
	ds_read_b128 v[182:185], v3 offset:4608
	v_mfma_f32_32x32x16_bf16 v[18:33], v[178:181], v[210:213], v[18:33]
	v_exp_f32_e32 v50, v98
	v_exp_f32_e32 v51, v99
	v_exp_f32_e32 v52, v100
	v_exp_f32_e32 v53, v101
	ds_read_b128 v[190:193], v3 offset:6144
	ds_read_b128 v[170:173], v3 offset:6656
	v_mfma_f32_32x32x16_bf16 v[34:49], v[178:181], v[12:15], v[34:49]
	v_exp_f32_e32 v54, v102
	v_exp_f32_e32 v55, v103
	v_exp_f32_e32 v56, v104
	v_exp_f32_e32 v57, v105
	ds_read_b128 v[178:181], v3 offset:8192
	ds_read_b128 v[166:169], v3 offset:8704
	v_mfma_f32_32x32x16_bf16 v[18:33], v[218:221], v[8:11], v[18:33]
	v_exp_f32_e32 v58, v106
	v_exp_f32_e32 v59, v107
	v_exp_f32_e32 v60, v108
	v_exp_f32_e32 v61, v109
	ds_read_b128 v[174:177], v3 offset:10240
	ds_read_b128 v[162:165], v3 offset:10752
	v_mfma_f32_32x32x16_bf16 v[34:49], v[218:221], v[4:7], v[34:49]
	v_exp_f32_e32 v62, v110
	v_exp_f32_e32 v63, v111
	v_exp_f32_e32 v64, v112
	v_exp_f32_e32 v65, v113
	s_add_i32 m0, s52, 0x1000
	s_and_b32 s64, s26, 3
	global_load_lds_dwordx4 v241, s[46:47]
	s_add_i32 m0, s53, 0x1000
	s_mulk_i32 s64, 0x3000
	global_load_lds_dwordx4 v241, s[60:61]
	s_add_i32 s52, s64, s91
	s_add_i32 s64, s42, 0x6000
	s_and_b32 s64, s64, 0x6000
	s_add_i32 s53, s64, s93
	s_add_u32 s46, s46, s62
	s_addc_u32 s47, s47, s63
	s_add_u32 s98, s98, s62
	s_addc_u32 s99, s99, s63
	s_add_u32 s60, s60, 0x2000
	s_addc_u32 s61, s61, 0
	s_mov_b32 s26, s27
	s_cmp_eq_u32 s27, s96
	s_cbranch_scc1 .Lmla_ss1_xdone
	s_add_i32 s64, s27, 3
	s_cmp_lt_u32 s64, s94
	s_cbranch_scc1 .Lmla_ss1_top
	s_waitcnt vmcnt(6)
	s_barrier
	s_branch .Lmla_ss_back
